# P3 queue: the last batch's attention items are taken heavy-to-light (head index flipped for items >= 896) so the mixer phase ends on short items instead of the longest ones
# speedup vs baseline: 1.0090x; 1.0090x over previous
.LBB0_500:
	s_andn2_b64 vcc, exec, s[8:9]
	s_cbranch_vccnz .LBB0_411
	s_cmpk_gt_i32 s54, 0x3ff
	s_mov_b64 s[6:7], 0
	s_cbranch_scc1 .LBB0_410
	s_cmpk_lt_i32 s54, 0x380
	s_cbranch_scc1 .Lmy_norev
	s_xor_b32 s54, s54, 0x70
.Lmy_norev:
	s_ashr_i32 s0, s54, 31
	s_lshr_b32 s1, s0, 28
	s_add_i32 s1, s54, s1
	s_ashr_i32 s6, s1, 4
	s_and_b32 s1, s1, 0x1fffff0
	s_sub_i32 s8, s54, s1
	s_lshr_b32 s1, s6, 29
	s_add_i32 s1, s6, s1
	s_and_b32 s1, s1, -8
	s_sub_i32 s10, s6, s1
	s_lshr_b32 s0, s0, 25
	s_add_i32 s54, s54, s0
	s_add_i32 s0, s10, 1
	v_cvt_f32_i32_e32 v2, s0
	s_mov_b32 s0, 0x42fc0000
	s_ashr_i32 s6, s54, 7
	v_mov_b32_e32 v82, v0
	v_cmp_lt_f32_e32 vcc, s0, v2
	s_and_b64 s[0:1], vcc, exec
	s_cselect_b32 s0, 0xffffffc0, 0
	v_cndmask_b32_e32 v4, 0, v214, vcc
	v_sub_f32_e32 v2, v4, v2
	v_exp_f32_e32 v2, v2
	s_ashr_i32 s7, s6, 31
	s_lshl_b32 s35, s8, 7
	s_mov_b32 s37, s55
	v_ldexp_f32 v4, v2, s0
	s_lshl_b64 s[0:1], s[6:7], 11
	s_ashr_i32 s7, s35, 31
	s_add_u32 s86, s0, s35
	s_addc_u32 s87, s1, s7
	s_mul_i32 s0, s87, 0x2c00
	s_mul_hi_u32 s1, s86, 0x2c00
	s_add_i32 s1, s1, s0
	s_mul_i32 s0, s86, 0x2c00
	s_add_u32 s7, s24, s0
	s_addc_u32 s8, s25, s1
	s_lshl_b32 s0, s10, 7
	s_ashr_i32 s1, s0, 31
	s_lshl_b64 s[88:89], s[0:1], 1
	s_add_u32 s0, s7, s88
	s_addc_u32 s1, s8, s89
	s_add_u32 s8, s0, 0x1400
	s_addc_u32 s9, s1, 0
	v_readfirstlane_b32 s55, v82
	s_ashr_i32 s82, s55, 7
	s_ashr_i32 s54, s55, 6
	v_and_b32_e32 v216, 31, v82
	s_lshl_b32 s0, s82, 5
	s_and_b32 s1, s54, 1
	v_or_b32_e32 v2, s0, v216
	v_mov_b64_e32 v[6:7], s[8:9]
	s_movk_i32 s7, 0x2c00
	v_bfe_u32 v221, v82, 5, 1
	v_mad_i64_i32 v[6:7], s[8:9], v2, s7, v[6:7]
	s_lshl_b32 s40, s1, 7
	v_lshl_add_u64 v[6:7], v[6:7], 0, s[40:41]
	v_lshlrev_b32_e32 v2, 4, v221
	v_lshl_add_u64 v[6:7], v[6:7], 0, v[2:3]
	s_lshl_b32 s44, s6, 3
	s_add_i32 s44, s44, s10
	s_ashr_i32 s45, s44, 31
	s_lshl_b64 s[44:45], s[44:45], 8
	v_readlane_b32 s46, v255, 13
	v_readlane_b32 s47, v255, 14
	v_and_b32_e32 v241, 63, v82
	s_add_u32 s44, s46, s44
	s_addc_u32 s45, s47, s45
	v_lshlrev_b32_e32 v241, 2, v241
	global_load_dword v240, v241, s[44:45] sc1
	global_load_dwordx4 v[130:133], v[6:7], off
	global_load_dwordx4 v[134:137], v[6:7], off offset:32
	global_load_dwordx4 v[138:141], v[6:7], off offset:64
	global_load_dwordx4 v[142:145], v[6:7], off offset:96
	v_and_b32_e32 v223, 63, v82
	s_barrier
	s_waitcnt vmcnt(3)
	v_and_b32_e32 v5, 0xffff0000, v130
	v_lshlrev_b32_e32 v2, 16, v130
	v_mul_f32_e32 v6, v5, v5
	v_fmac_f32_e32 v6, v2, v2
	v_lshlrev_b32_e32 v2, 16, v131
	v_fmac_f32_e32 v6, v2, v2
	v_and_b32_e32 v2, 0xffff0000, v131
	v_fmac_f32_e32 v6, v2, v2
	v_lshlrev_b32_e32 v2, 16, v132
	v_fmac_f32_e32 v6, v2, v2
	v_and_b32_e32 v2, 0xffff0000, v132
	v_fmac_f32_e32 v6, v2, v2
	v_lshlrev_b32_e32 v2, 16, v133
	v_fmac_f32_e32 v6, v2, v2
	v_and_b32_e32 v2, 0xffff0000, v133
	v_fmac_f32_e32 v6, v2, v2
	s_waitcnt vmcnt(2)
	v_lshlrev_b32_e32 v2, 16, v134
	v_fmac_f32_e32 v6, v2, v2
	v_and_b32_e32 v2, 0xffff0000, v134
	v_fmac_f32_e32 v6, v2, v2
	v_lshlrev_b32_e32 v2, 16, v135
	v_fmac_f32_e32 v6, v2, v2
	v_and_b32_e32 v2, 0xffff0000, v135
	v_fmac_f32_e32 v6, v2, v2
	v_lshlrev_b32_e32 v2, 16, v136
	v_fmac_f32_e32 v6, v2, v2
	v_and_b32_e32 v2, 0xffff0000, v136
	v_fmac_f32_e32 v6, v2, v2
	v_lshlrev_b32_e32 v2, 16, v137
	v_fmac_f32_e32 v6, v2, v2
	v_and_b32_e32 v2, 0xffff0000, v137
	v_fmac_f32_e32 v6, v2, v2
	s_waitcnt vmcnt(1)
	v_lshlrev_b32_e32 v2, 16, v138
	v_fmac_f32_e32 v6, v2, v2
	v_and_b32_e32 v2, 0xffff0000, v138
	v_fmac_f32_e32 v6, v2, v2
	v_lshlrev_b32_e32 v2, 16, v139
	v_fmac_f32_e32 v6, v2, v2
	v_and_b32_e32 v2, 0xffff0000, v139
	v_fmac_f32_e32 v6, v2, v2
	v_lshlrev_b32_e32 v2, 16, v140
	v_fmac_f32_e32 v6, v2, v2
	v_and_b32_e32 v2, 0xffff0000, v140
	v_fmac_f32_e32 v6, v2, v2
	v_lshlrev_b32_e32 v2, 16, v141
	v_fmac_f32_e32 v6, v2, v2
	v_and_b32_e32 v2, 0xffff0000, v141
	v_fmac_f32_e32 v6, v2, v2
	s_waitcnt vmcnt(0)
	v_lshlrev_b32_e32 v2, 16, v142
	v_fmac_f32_e32 v6, v2, v2
	v_and_b32_e32 v2, 0xffff0000, v142
	v_fmac_f32_e32 v6, v2, v2
	v_lshlrev_b32_e32 v2, 16, v143
	v_fmac_f32_e32 v6, v2, v2
	v_and_b32_e32 v2, 0xffff0000, v143
	v_fmac_f32_e32 v6, v2, v2
	v_lshlrev_b32_e32 v2, 16, v144
	v_fmac_f32_e32 v6, v2, v2
	v_and_b32_e32 v2, 0xffff0000, v144
	v_fmac_f32_e32 v6, v2, v2
	v_lshlrev_b32_e32 v2, 16, v145
	v_fmac_f32_e32 v6, v2, v2
	v_and_b32_e32 v2, 0xffff0000, v145
	v_and_b32_e32 v5, 64, v212
	v_fmac_f32_e32 v6, v2, v2
	v_xor_b32_e32 v2, 32, v212
	v_add_u32_e32 v5, 64, v5
	v_cmp_lt_i32_e32 vcc, v2, v5
	s_nop 1
	v_cndmask_b32_e32 v2, v212, v2, vcc
	v_lshlrev_b32_e32 v2, 2, v2
	v_mov_b32_e32 v7, v6
	s_nop 1
	v_permlane32_swap_b32_e32 v7, v6
	s_waitcnt lgkmcnt(0)
	v_add_f32_e32 v6, v6, v7
	v_xor_b32_e32 v7, 16, v212
	v_cmp_lt_i32_e32 vcc, v7, v5
	s_nop 1
	v_cndmask_b32_e32 v7, v212, v7, vcc
	v_lshlrev_b32_e32 v217, 2, v7
	v_mov_b32_e32 v7, v6
	s_nop 1
	v_permlane16_swap_b32_e32 v7, v6
	s_waitcnt lgkmcnt(0)
	v_max_f32_e32 v7, v7, v7
	v_max_f32_e32 v6, v6, v7
	v_xor_b32_e32 v7, 8, v212
	v_cmp_lt_i32_e32 vcc, v7, v5
	s_nop 1
	v_cndmask_b32_e32 v7, v212, v7, vcc
	v_lshlrev_b32_e32 v218, 2, v7
	s_nop 1
	v_mov_b32_dpp v7, v6 row_ror:8 row_mask:0xf bank_mask:0xf
	s_waitcnt lgkmcnt(0)
	v_max_f32_e32 v7, v7, v7
	v_max_f32_e32 v6, v6, v7
	v_xor_b32_e32 v7, 4, v212
	v_cmp_lt_i32_e32 vcc, v7, v5
	s_nop 1
	v_cndmask_b32_e32 v7, v212, v7, vcc
	v_lshlrev_b32_e32 v219, 2, v7
	s_nop 1
	v_mov_b32_dpp v7, v6 row_shr:4 row_mask:0xf bank_mask:0xa
	v_mov_b32_dpp v7, v6 row_shl:4 row_mask:0xf bank_mask:0x5
	s_waitcnt lgkmcnt(0)
	v_max_f32_e32 v7, v7, v7
	v_max_f32_e32 v6, v6, v7
	v_xor_b32_e32 v7, 2, v212
	v_cmp_lt_i32_e32 vcc, v7, v5
	s_nop 1
	v_cndmask_b32_e32 v7, v212, v7, vcc
	v_lshlrev_b32_e32 v220, 2, v7
	s_nop 1
	v_mov_b32_dpp v7, v6 quad_perm:[2,3,0,1] row_mask:0xf bank_mask:0xf
	s_waitcnt lgkmcnt(0)
	v_max_f32_e32 v7, v7, v7
	v_max_f32_e32 v6, v6, v7
	v_xor_b32_e32 v7, 1, v212
	v_cmp_lt_i32_e32 vcc, v7, v5
	s_nop 1
	v_cndmask_b32_e32 v5, v212, v7, vcc
	v_lshlrev_b32_e32 v222, 2, v5
	s_nop 1
	v_mov_b32_dpp v5, v6 quad_perm:[1,0,3,2] row_mask:0xf bank_mask:0xf
	v_cmp_eq_u32_e32 vcc, 0, v223
	s_and_saveexec_b64 s[8:9], vcc
	s_cbranch_execz .LBB0_504
	s_lshl_b32 s7, s54, 2
	s_add_i32 s7, s7, 0
	s_waitcnt lgkmcnt(0)
	v_max_f32_e32 v5, v5, v5
	v_max_f32_e32 v6, v6, v6
	s_add_i32 s7, s7, 0x18c00
	v_max_f32_e32 v5, v6, v5
	v_mov_b32_e32 v6, s7
	ds_write_b32 v6, v5
